# P3 (gate + merged) and P4 GEMM K-loops: LDS-DMA issue balanced 4/4/4/4 over the load segments (B pieces 2,3 one segment later)
# baseline (speedup 1.0000x reference)
; #define PG8_STAGE_B(bufoff, gbase) do { _Pragma("unroll") for (int _i = 0; _i < 2; ++_i) \
;         __builtin_amdgcn_global_load_lds((const unsigned*)((const char*)(gbase) + voffB[_i]), (LAS unsigned*)(lds + (bufoff) + ldsw + _i * 8192), 16, 0, 0); } while (0)
; #define PG8_STAGE_A(bufoff, gbase, VO, h) do { _Pragma("unroll") for (int _i = 0; _i < 2; ++_i) \
;         __builtin_amdgcn_global_load_lds((const unsigned*)((const char*)(gbase) + (VO)[h][_i]), (LAS unsigned*)(lds + (bufoff) + ldsw + _i * 8192), 16, 0, 0); } while (0)
; #define PG8_WAIT_V(n) asm volatile("s_waitcnt vmcnt(" #n ")" ::: "memory")
; #define PG8_BAR __builtin_amdgcn_s_barrier()
;     ...
;     for (int i = 0; i < 2; ++i) { int R, C; stage_rc(tid * 16 + i * 8192, R, C); const int Rb = (R & ~31) + perm32(R & 31);
;         Rr[i] = R; Cc[i] = C; voffB[i] = nB64 ? (unsigned)(Rb * 64 + ((C * 2) & 63) + ((C * 2) >> 6) * nB64 * 64) : (unsigned)(Rb * ldb + C) * 2u;
;         voffA[0][i] = (unsigned)(R * lda + C) * 2u; voffA[1][i] = (unsigned)((R + HALF) * lda + C) * 2u; voffN[0][i] = voffA[0][i]; voffN[1][i] = voffA[1][i]; }
;     const size_t kstep = (size_t)(BK * 2);
;     const size_t kstepB = kstepB_arg ? kstepB_arg : kstep;
;     const size_t hstepB = nB64 ? (size_t)HALF * 64 : (size_t)HALF * ldb * 2;
;     const unsigned ldsw = (unsigned)wid * 1024u;
;     const int aoff = lds_byte(wr * 64 + fr, fq * 8), boff = lds_byte(wc * 32 + fr, fq * 8);
;     ...
;     PG8_STAGE_B(PG8_SB(0, 0), cB); PG8_STAGE_B(PG8_SB(0, 1), cB + hstepB); PG8_STAGE_A(PG8_SA(0, 0), cA, voffA, 0); PG8_STAGE_A(PG8_SA(0, 1), cA, voffA, 1);
;     if (wr == 1) PG8_BAR;
;     PG8_WAIT_V(2); PG8_BAR;
;     PG8_STAGE_B(PG8_SB(1, 0), cB + kstepB); PG8_STAGE_A(PG8_SA(1, 0), cA + kstep, voffA, 0); PG8_STAGE_B(PG8_SB(1, 1), cB + hstepB + kstepB);
;     PG8_WAIT_V(6); PG8_BAR;
.LBB0_613:
	s_mul_i32 s6, s60, 0x6000
	v_readlane_b32 s8, v249, 11
	s_add_u32 s6, s8, s6
	v_and_b32_e32 v13, 15, v12
	v_readlane_b32 s8, v249, 41
	v_lshrrev_b32_e32 v14, 1, v12
	v_and_b32_e32 v14, 24, v14
	v_or_b32_e32 v216, s8, v13
	v_lshlrev_b32_e32 v15, 6, v216
	v_lshlrev_b32_e32 v16, 1, v14
	s_movk_i32 s8, 0x3c0
	v_lshlrev_b32_e32 v17, 2, v216
	v_readlane_b32 s9, v249, 12
	v_and_or_b32 v15, v15, s8, v16
	v_and_b32_e32 v17, 32, v17
	v_readlane_b32 s8, v249, 42
	v_lshlrev_b32_e32 v12, 2, v12
	s_addc_u32 s7, s9, 0
	v_bitop3_b32 v15, v15, s8, v17 bitop3:0xde
	v_lshl_or_b32 v13, v13, 6, v16
	v_and_b32_e32 v12, 32, v12
	v_readlane_b32 s8, v249, 44
	v_mov_b32_e32 v195, v65
	v_mov_b32_e32 v199, v65
	v_bitop3_b32 v16, v13, s8, v12 bitop3:0xde
	s_add_u32 s8, s2, 0x180000
	s_addc_u32 s9, s3, 0
	s_add_i32 s35, s24, 0x18000
	v_lshl_add_u64 v[12:13], s[8:9], 0, v[194:195]
	s_mov_b32 m0, s35
	s_add_i32 s36, s24, 0x1a000
	s_waitcnt vmcnt(2)
	s_barrier
	global_load_lds_dwordx4 v[12:13], off
	v_lshl_add_u64 v[12:13], s[8:9], 0, v[198:199]
	s_mov_b32 m0, s36
	s_add_i32 s37, s24, 0x8000
	s_add_i32 s40, s24, 0xa000
	global_load_lds_dwordx4 v[12:13], off
	v_lshl_add_u64 v[0:1], v[0:1], 0, s[94:95]
	s_mov_b32 m0, s37
	s_add_u32 s8, s2, 0x182000
	global_load_lds_dwordx4 v[0:1], off
	v_lshl_add_u64 v[0:1], v[2:3], 0, s[94:95]
	s_mov_b32 m0, s40
	s_addc_u32 s9, s3, 0
	s_add_i32 s41, s24, 0x1c000
	global_load_lds_dwordx4 v[0:1], off
	v_lshl_add_u64 v[232:233], s[8:9], 0, v[194:195]
	s_add_i32 s42, s24, 0x1e000
	v_lshl_add_u64 v[234:235], s[8:9], 0, v[198:199]
	v_readlane_b32 s8, v249, 43
	v_lshlrev_b32_e32 v0, 13, v8
	v_and_b32_e32 v0, 0x7fffc000, v0
	v_lshl_add_u32 v0, v9, 10, v0
	v_or_b32_e32 v0, v0, v10
	v_add_u32_sdwa v0, v0, sext(v11) dst_sel:DWORD dst_unused:UNUSED_PAD src0_sel:DWORD src1_sel:WORD_0
	v_mov_b32_e32 v1, 0x40000
	v_lshl_add_u32 v204, v0, 1, v1
	v_lshlrev_b32_e32 v0, 13, v4
	v_and_b32_e32 v0, 0x7fffc000, v0
	v_lshl_add_u32 v0, v5, 10, v0
	s_waitcnt vmcnt(4)
	v_or_b32_e32 v0, v0, v6
	v_add_u32_sdwa v0, v0, sext(v7) dst_sel:DWORD dst_unused:UNUSED_PAD src0_sel:DWORD src1_sel:WORD_0
	v_mov_b32_e32 v197, v65
	v_mov_b32_e32 v203, v65
	v_or_b32_e32 v217, s8, v14
	v_mov_b32_e32 v205, v65
	v_lshl_add_u32 v206, v0, 1, v1
	v_mov_b32_e32 v207, v65
	s_mov_b32 s43, 0
	s_mov_b64 s[12:13], 0
	v_add_u32_e32 v218, 0, v16
	v_add_u32_e32 v219, 0, v15
	s_mov_b64 s[8:9], s[4:5]
	s_mov_b64 s[10:11], s[2:3]
	s_barrier
	s_branch .LBB0_616

; #define PG8_STAGE_B(bufoff, gbase) do { _Pragma("unroll") for (int _i = 0; _i < 2; ++_i) \
;         __builtin_amdgcn_global_load_lds((const unsigned*)((const char*)(gbase) + voffB[_i]), (LAS unsigned*)(lds + (bufoff) + ldsw + _i * 8192), 16, 0, 0); } while (0)
; #define PG8_STAGE_A(bufoff, gbase, VO, h) do { _Pragma("unroll") for (int _i = 0; _i < 2; ++_i) \
;         __builtin_amdgcn_global_load_lds((const unsigned*)((const char*)(gbase) + (VO)[h][_i]), (LAS unsigned*)(lds + (bufoff) + ldsw + _i * 8192), 16, 0, 0); } while (0)
; #define PG8_WAIT_V(n) asm volatile("s_waitcnt vmcnt(" #n ")" ::: "memory")
; #define PG8_WAIT_L(n) asm volatile("s_waitcnt lgkmcnt(" #n ")" ::: "memory")
; #define PG8_WAIT_VX(rx) do { if (rx) asm volatile("s_waitcnt vmcnt(%0)" :: "n"(8 + Epi::NVM) : "memory"); else asm volatile("s_waitcnt vmcnt(8)" ::: "memory"); } while (0)
; #define PG8_BAR __builtin_amdgcn_s_barrier()
; #define PG8_SCHED __builtin_amdgcn_sched_barrier(0)
;     ...
;             PG8_WAIT_VX(rx); PG8_WAIT_L(0); PG8_BAR; PG8_MMA(0, 0, At, B0); PG8_MMA(0, 1, At, B1); PG8_BAR; PG8_SCHED;
;             PG8_LDA(At, 1, 1); PG8_STAGE_B(PG8_SB(1, 0), b3); PG8_STAGE_B(PG8_SB(1, 1), b3 + hstepB); PG8_STAGE_A(PG8_SA(1, 0), a3, vo2, 0);
;             PG8_WAIT_V(8); PG8_WAIT_L(0); PG8_BAR; PG8_MMA(1, 0, At, B0); PG8_MMA(1, 1, At, B1); PG8_BAR; PG8_SCHED;
.LBB0_623:
	s_waitcnt lgkmcnt(0)
	s_add_u32 s2, s18, 0x180000
	s_addc_u32 s3, s19, 0
	s_barrier
	s_setprio 1
	s_waitcnt lgkmcnt(0)
	v_mfma_scale_f32_16x16x128_f8f6f4 v[190:193], v[24:31], v[56:63], v[190:193], v226, v225 op_sel_hi:[0,0,0]
	v_mfma_scale_f32_16x16x128_f8f6f4 v[186:189], v[16:23], v[56:63], v[186:189], v226, v225 op_sel_hi:[0,0,0]
	v_mfma_scale_f32_16x16x128_f8f6f4 v[174:177], v[24:31], v[48:55], v[174:177], v226, v225 op_sel_hi:[0,0,0]
	v_mfma_scale_f32_16x16x128_f8f6f4 v[170:173], v[16:23], v[48:55], v[170:173], v226, v225 op_sel_hi:[0,0,0]
	v_mfma_scale_f32_16x16x128_f8f6f4 v[158:161], v[24:31], v[40:47], v[158:161], v226, v225 op_sel_hi:[0,0,0]
	v_mfma_scale_f32_16x16x128_f8f6f4 v[154:157], v[16:23], v[40:47], v[154:157], v226, v225 op_sel_hi:[0,0,0]
	v_mfma_scale_f32_16x16x128_f8f6f4 v[142:145], v[24:31], v[32:39], v[142:145], v226, v225 op_sel_hi:[0,0,0]
	v_mfma_scale_f32_16x16x128_f8f6f4 v[138:141], v[16:23], v[32:39], v[138:141], v226, v225 op_sel_hi:[0,0,0]
	s_setprio 0
	s_setprio 1
	v_mfma_scale_f32_16x16x128_f8f6f4 v[182:185], v[8:15], v[56:63], v[182:185], v226, v225 op_sel_hi:[0,0,0]
	v_mfma_scale_f32_16x16x128_f8f6f4 v[178:181], v[0:7], v[56:63], v[178:181], v226, v225 op_sel_hi:[0,0,0]
	v_mfma_scale_f32_16x16x128_f8f6f4 v[166:169], v[8:15], v[48:55], v[166:169], v226, v225 op_sel_hi:[0,0,0]
	v_mfma_scale_f32_16x16x128_f8f6f4 v[162:165], v[0:7], v[48:55], v[162:165], v226, v225 op_sel_hi:[0,0,0]
	v_mfma_scale_f32_16x16x128_f8f6f4 v[150:153], v[8:15], v[40:47], v[150:153], v226, v225 op_sel_hi:[0,0,0]
	v_mfma_scale_f32_16x16x128_f8f6f4 v[146:149], v[0:7], v[40:47], v[146:149], v226, v225 op_sel_hi:[0,0,0]
	v_mfma_scale_f32_16x16x128_f8f6f4 v[134:137], v[8:15], v[32:39], v[134:137], v226, v225 op_sel_hi:[0,0,0]
	v_mfma_scale_f32_16x16x128_f8f6f4 v[130:133], v[0:7], v[32:39], v[130:133], v226, v225 op_sel_hi:[0,0,0]
	s_setprio 0
	s_barrier
	s_mov_b32 m0, s35
	v_lshl_add_u64 v[220:221], s[2:3], 0, v[194:195]
	ds_read_b128 v[32:35], v219 offset:49152
	ds_read_b128 v[36:39], v219 offset:50176
	ds_read_b128 v[40:43], v219 offset:51200
	ds_read_b128 v[44:47], v219 offset:52224
	ds_read_b128 v[48:51], v219 offset:53248
	ds_read_b128 v[52:55], v219 offset:54272
	ds_read_b128 v[56:59], v219 offset:55296
	ds_read_b128 v[60:63], v219 offset:56320
	global_load_lds_dwordx4 v[220:221], off
	v_lshl_add_u64 v[220:221], s[2:3], 0, v[198:199]
	s_add_u32 s2, s18, 0x182000
	s_mov_b32 m0, s36
	s_addc_u32 s3, s19, 0
	global_load_lds_dwordx4 v[220:221], off
	v_lshl_add_u64 v[232:233], s[2:3], 0, v[194:195]
	v_lshl_add_u64 v[212:213], v[212:213], 0, s[94:95]
	v_lshl_add_u64 v[234:235], s[2:3], 0, v[198:199]
	s_mov_b32 m0, s37
	s_nop 0
	global_load_lds_dwordx4 v[212:213], off
	v_lshl_add_u64 v[212:213], v[214:215], 0, s[94:95]
	s_mov_b32 m0, s40
	s_nop 0
	global_load_lds_dwordx4 v[212:213], off
	s_waitcnt vmcnt(6)
	s_waitcnt lgkmcnt(0)
	s_barrier
	s_setprio 1
	s_waitcnt lgkmcnt(0)
	v_mfma_scale_f32_16x16x128_f8f6f4 v[126:129], v[24:31], v[32:39], v[126:129], v226, v225 op_sel_hi:[0,0,0]
	v_mfma_scale_f32_16x16x128_f8f6f4 v[122:125], v[16:23], v[32:39], v[122:125], v226, v225 op_sel_hi:[0,0,0]
	v_mfma_scale_f32_16x16x128_f8f6f4 v[110:113], v[24:31], v[40:47], v[110:113], v226, v225 op_sel_hi:[0,0,0]
	v_mfma_scale_f32_16x16x128_f8f6f4 v[106:109], v[16:23], v[40:47], v[106:109], v226, v225 op_sel_hi:[0,0,0]
	v_mfma_scale_f32_16x16x128_f8f6f4 v[94:97], v[24:31], v[48:55], v[94:97], v226, v225 op_sel_hi:[0,0,0]
	v_mfma_scale_f32_16x16x128_f8f6f4 v[86:89], v[16:23], v[48:55], v[86:89], v226, v225 op_sel_hi:[0,0,0]
	v_mfma_scale_f32_16x16x128_f8f6f4 v[78:81], v[24:31], v[56:63], v[78:81], v226, v225 op_sel_hi:[0,0,0]
	v_mfma_scale_f32_16x16x128_f8f6f4 v[66:69], v[16:23], v[56:63], v[66:69], v226, v225 op_sel_hi:[0,0,0]
	s_setprio 0
	s_setprio 1
	v_mfma_scale_f32_16x16x128_f8f6f4 v[118:121], v[8:15], v[32:39], v[118:121], v226, v225 op_sel_hi:[0,0,0]
	v_mfma_scale_f32_16x16x128_f8f6f4 v[114:117], v[0:7], v[32:39], v[114:117], v226, v225 op_sel_hi:[0,0,0]
	v_mfma_scale_f32_16x16x128_f8f6f4 v[102:105], v[8:15], v[40:47], v[102:105], v226, v225 op_sel_hi:[0,0,0]
	v_mfma_scale_f32_16x16x128_f8f6f4 v[98:101], v[0:7], v[40:47], v[98:101], v226, v225 op_sel_hi:[0,0,0]
	v_mfma_scale_f32_16x16x128_f8f6f4 v[90:93], v[8:15], v[48:55], v[90:93], v226, v225 op_sel_hi:[0,0,0]
	v_mfma_scale_f32_16x16x128_f8f6f4 v[82:85], v[0:7], v[48:55], v[82:85], v226, v225 op_sel_hi:[0,0,0]
	v_mfma_scale_f32_16x16x128_f8f6f4 v[74:77], v[8:15], v[56:63], v[74:77], v226, v225 op_sel_hi:[0,0,0]
	v_mfma_scale_f32_16x16x128_f8f6f4 v[70:73], v[0:7], v[56:63], v[70:73], v226, v225 op_sel_hi:[0,0,0]
	s_setprio 0
	s_barrier
	s_add_i32 s50, s50, 2
	s_add_u32 s48, s48, 0x300000
	s_addc_u32 s49, s49, 0
	s_add_u32 s16, s16, 0x100
	s_addc_u32 s17, s17, 0
	s_cmp_gt_u32 s50, 13
	s_cbranch_scc1 .LBB0_636

; #define PG8_STAGE_B(bufoff, gbase) do { _Pragma("unroll") for (int _i = 0; _i < 2; ++_i) \
;         __builtin_amdgcn_global_load_lds((const unsigned*)((const char*)(gbase) + voffB[_i]), (LAS unsigned*)(lds + (bufoff) + ldsw + _i * 8192), 16, 0, 0); } while (0)
; #define PG8_STAGE_A(bufoff, gbase, VO, h) do { _Pragma("unroll") for (int _i = 0; _i < 2; ++_i) \
;         __builtin_amdgcn_global_load_lds((const unsigned*)((const char*)(gbase) + (VO)[h][_i]), (LAS unsigned*)(lds + (bufoff) + ldsw + _i * 8192), 16, 0, 0); } while (0)
; #define PG8_WAIT_L(n) asm volatile("s_waitcnt lgkmcnt(" #n ")" ::: "memory")
; #define PG8_WAIT_VX(rx) do { if (rx) asm volatile("s_waitcnt vmcnt(%0)" :: "n"(8 + Epi::NVM) : "memory"); else asm volatile("s_waitcnt vmcnt(8)" ::: "memory"); } while (0)
; #define PG8_BAR __builtin_amdgcn_s_barrier()
; #define PG8_SCHED __builtin_amdgcn_sched_barrier(0)
;     ...
;             PG8_LDB(B0, 0, 0); PG8_LDB(B1, 0, 1); PG8_SCHED; PG8_LDA(At, 0, 0); if (!rx) PG8_STAGE_A(PG8_SA(1, 1), a1, voffA, 1);
;             PG8_WAIT_VX(rx); PG8_WAIT_L(0); PG8_BAR; PG8_MMA(0, 0, At, B0); PG8_MMA(0, 1, At, B1); PG8_BAR; PG8_SCHED;
;             PG8_LDA(At, 0, 1); PG8_STAGE_B(PG8_SB(0, 0), b2); PG8_STAGE_B(PG8_SB(0, 1), b2 + hstepB); PG8_STAGE_A(PG8_SA(0, 0), a2, vo2, 0);
.LBB0_626:
	s_mov_b32 m0, s41
	s_nop 0
	global_load_lds_dwordx4 v[232:233], off
	s_mov_b32 m0, s42
	s_nop 0
	global_load_lds_dwordx4 v[234:235], off
	v_lshl_add_u64 v[212:213], v[210:211], 0, s[16:17]
	s_add_i32 m0, s24, 0xc000
	s_nop 0
	global_load_lds_dwordx4 v[212:213], off
	v_lshl_add_u64 v[212:213], v[208:209], 0, s[16:17]
	s_add_i32 m0, s24, 0xe000
	s_nop 0
	global_load_lds_dwordx4 v[212:213], off
	s_waitcnt vmcnt(8)
.LBB0_627:
	s_add_u32 s2, s4, s16
	s_addc_u32 s3, s5, s17
	s_add_u32 s2, s2, 0x100
	s_addc_u32 s3, s3, 0
	s_waitcnt lgkmcnt(0)
	s_cmpk_eq_i32 s16, 0x700
	s_cselect_b32 s21, s9, s3
	s_cselect_b32 s20, s8, s2
	s_cselect_b32 s19, s11, s49
	s_cselect_b32 s18, s10, s48
	s_barrier
	s_setprio 1
	s_waitcnt lgkmcnt(0)
	v_mfma_scale_f32_16x16x128_f8f6f4 v[190:193], v[24:31], v[56:63], v[190:193], v226, v225 op_sel_hi:[0,0,0]
	v_mfma_scale_f32_16x16x128_f8f6f4 v[186:189], v[16:23], v[56:63], v[186:189], v226, v225 op_sel_hi:[0,0,0]
	v_mfma_scale_f32_16x16x128_f8f6f4 v[174:177], v[24:31], v[48:55], v[174:177], v226, v225 op_sel_hi:[0,0,0]
	v_mfma_scale_f32_16x16x128_f8f6f4 v[170:173], v[16:23], v[48:55], v[170:173], v226, v225 op_sel_hi:[0,0,0]
	v_mfma_scale_f32_16x16x128_f8f6f4 v[158:161], v[24:31], v[40:47], v[158:161], v226, v225 op_sel_hi:[0,0,0]
	v_mfma_scale_f32_16x16x128_f8f6f4 v[154:157], v[16:23], v[40:47], v[154:157], v226, v225 op_sel_hi:[0,0,0]
	v_mfma_scale_f32_16x16x128_f8f6f4 v[142:145], v[24:31], v[32:39], v[142:145], v226, v225 op_sel_hi:[0,0,0]
	v_mfma_scale_f32_16x16x128_f8f6f4 v[138:141], v[16:23], v[32:39], v[138:141], v226, v225 op_sel_hi:[0,0,0]
	s_setprio 0
	s_setprio 1
	v_mfma_scale_f32_16x16x128_f8f6f4 v[182:185], v[8:15], v[56:63], v[182:185], v226, v225 op_sel_hi:[0,0,0]
	v_mfma_scale_f32_16x16x128_f8f6f4 v[178:181], v[0:7], v[56:63], v[178:181], v226, v225 op_sel_hi:[0,0,0]
	v_mfma_scale_f32_16x16x128_f8f6f4 v[166:169], v[8:15], v[48:55], v[166:169], v226, v225 op_sel_hi:[0,0,0]
	v_mfma_scale_f32_16x16x128_f8f6f4 v[162:165], v[0:7], v[48:55], v[162:165], v226, v225 op_sel_hi:[0,0,0]
	v_mfma_scale_f32_16x16x128_f8f6f4 v[150:153], v[8:15], v[40:47], v[150:153], v226, v225 op_sel_hi:[0,0,0]
	v_mfma_scale_f32_16x16x128_f8f6f4 v[146:149], v[0:7], v[40:47], v[146:149], v226, v225 op_sel_hi:[0,0,0]
	v_mfma_scale_f32_16x16x128_f8f6f4 v[134:137], v[8:15], v[32:39], v[134:137], v226, v225 op_sel_hi:[0,0,0]
	v_mfma_scale_f32_16x16x128_f8f6f4 v[130:133], v[0:7], v[32:39], v[130:133], v226, v225 op_sel_hi:[0,0,0]
	s_setprio 0
	s_barrier
	s_mov_b32 m0, s25
	v_lshl_add_u64 v[212:213], s[18:19], 0, v[194:195]
	s_add_u32 s2, s18, 0x2000
	ds_read_b128 v[56:59], v219 offset:16384
	ds_read_b128 v[60:63], v219 offset:17408
	ds_read_b128 v[48:51], v219 offset:18432
	ds_read_b128 v[52:55], v219 offset:19456
	ds_read_b128 v[40:43], v219 offset:20480
	ds_read_b128 v[44:47], v219 offset:21504
	ds_read_b128 v[32:35], v219 offset:22528
	ds_read_b128 v[36:39], v219 offset:23552
	global_load_lds_dwordx4 v[212:213], off
	v_lshl_add_u64 v[212:213], s[18:19], 0, v[198:199]
	s_mov_b32 m0, s26
	s_addc_u32 s3, s19, 0
	global_load_lds_dwordx4 v[212:213], off
	v_lshl_add_u64 v[232:233], s[2:3], 0, v[194:195]
	v_lshl_add_u64 v[214:215], s[20:21], 0, v[200:201]
	v_lshl_add_u64 v[234:235], s[2:3], 0, v[198:199]
	v_cndmask_b32_e64 v220, 0, 1, s[22:23]
	v_lshl_add_u64 v[212:213], s[20:21], 0, v[64:65]
	s_mov_b32 m0, s24
	v_cmp_ne_u32_e64 s[2:3], 1, v220
	global_load_lds_dwordx4 v[212:213], off
	s_mov_b32 m0, s29
	s_andn2_b64 vcc, exec, s[22:23]
	global_load_lds_dwordx4 v[214:215], off
	s_cbranch_vccnz .LBB0_633
	s_waitcnt vmcnt(22)
	s_cbranch_execnz .LBB0_630

; #define PG8_STAGE_A(bufoff, gbase, VO, h) do { _Pragma("unroll") for (int _i = 0; _i < 2; ++_i) \
;         __builtin_amdgcn_global_load_lds((const unsigned*)((const char*)(gbase) + (VO)[h][_i]), (LAS unsigned*)(lds + (bufoff) + ldsw + _i * 8192), 16, 0, 0); } while (0)
; #define PG8_WAIT_L(n) asm volatile("s_waitcnt lgkmcnt(" #n ")" ::: "memory")
; #define PG8_WAIT_VX(rx) do { if (rx) asm volatile("s_waitcnt vmcnt(%0)" :: "n"(8 + Epi::NVM) : "memory"); else asm volatile("s_waitcnt vmcnt(8)" ::: "memory"); } while (0)
; #define PG8_BAR __builtin_amdgcn_s_barrier()
; #define PG8_SCHED __builtin_amdgcn_sched_barrier(0)
;     ...
;             PG8_WAIT_VX(rx); PG8_WAIT_L(0); PG8_BAR; PG8_MMA(1, 0, At, B0); PG8_MMA(1, 1, At, B1); PG8_BAR; PG8_SCHED;
;             PG8_LDB(B0, 1, 0); PG8_LDB(B1, 1, 1); PG8_SCHED; PG8_LDA(At, 1, 0); PG8_STAGE_A(PG8_SA(0, 1), a2, vo2, 1);
.LBB0_630:
	s_waitcnt lgkmcnt(0)
	s_barrier
	s_setprio 1
	s_waitcnt lgkmcnt(0)
	v_mfma_scale_f32_16x16x128_f8f6f4 v[126:129], v[24:31], v[56:63], v[126:129], v226, v225 op_sel_hi:[0,0,0]
	v_mfma_scale_f32_16x16x128_f8f6f4 v[122:125], v[16:23], v[56:63], v[122:125], v226, v225 op_sel_hi:[0,0,0]
	v_mfma_scale_f32_16x16x128_f8f6f4 v[110:113], v[24:31], v[48:55], v[110:113], v226, v225 op_sel_hi:[0,0,0]
	v_mfma_scale_f32_16x16x128_f8f6f4 v[106:109], v[16:23], v[48:55], v[106:109], v226, v225 op_sel_hi:[0,0,0]
	v_mfma_scale_f32_16x16x128_f8f6f4 v[94:97], v[24:31], v[40:47], v[94:97], v226, v225 op_sel_hi:[0,0,0]
	v_mfma_scale_f32_16x16x128_f8f6f4 v[86:89], v[16:23], v[40:47], v[86:89], v226, v225 op_sel_hi:[0,0,0]
	v_mfma_scale_f32_16x16x128_f8f6f4 v[78:81], v[24:31], v[32:39], v[78:81], v226, v225 op_sel_hi:[0,0,0]
	v_mfma_scale_f32_16x16x128_f8f6f4 v[66:69], v[16:23], v[32:39], v[66:69], v226, v225 op_sel_hi:[0,0,0]
	s_setprio 0
	s_setprio 1
	v_mfma_scale_f32_16x16x128_f8f6f4 v[118:121], v[8:15], v[56:63], v[118:121], v226, v225 op_sel_hi:[0,0,0]
	v_mfma_scale_f32_16x16x128_f8f6f4 v[114:117], v[0:7], v[56:63], v[114:117], v226, v225 op_sel_hi:[0,0,0]
	v_mfma_scale_f32_16x16x128_f8f6f4 v[102:105], v[8:15], v[48:55], v[102:105], v226, v225 op_sel_hi:[0,0,0]
	v_mfma_scale_f32_16x16x128_f8f6f4 v[98:101], v[0:7], v[48:55], v[98:101], v226, v225 op_sel_hi:[0,0,0]
	v_mfma_scale_f32_16x16x128_f8f6f4 v[90:93], v[8:15], v[40:47], v[90:93], v226, v225 op_sel_hi:[0,0,0]
	v_mfma_scale_f32_16x16x128_f8f6f4 v[82:85], v[0:7], v[40:47], v[82:85], v226, v225 op_sel_hi:[0,0,0]
	v_mfma_scale_f32_16x16x128_f8f6f4 v[74:77], v[8:15], v[32:39], v[74:77], v226, v225 op_sel_hi:[0,0,0]
	v_mfma_scale_f32_16x16x128_f8f6f4 v[70:73], v[0:7], v[32:39], v[70:73], v226, v225 op_sel_hi:[0,0,0]
	s_setprio 0
	s_barrier
	v_add_u32_e32 v0, 0x18000, v218
	v_add_u32_e32 v4, 0x1c000, v218
	ds_read_b128 v[24:27], v0
	ds_read_b128 v[28:31], v0 offset:1024
	ds_read_b128 v[16:19], v0 offset:2048
	ds_read_b128 v[20:23], v0 offset:3072
	ds_read_b128 v[8:11], v4
	ds_read_b128 v[12:15], v4 offset:1024
	ds_read_b128 v[0:3], v4 offset:2048
	ds_read_b128 v[4:7], v4 offset:3072
	s_mov_b32 m0, s31
	v_lshl_add_u64 v[220:221], s[20:21], 0, v[196:197]
	ds_read_b128 v[56:59], v219 offset:32768
	ds_read_b128 v[60:63], v219 offset:33792
	ds_read_b128 v[48:51], v219 offset:34816
	ds_read_b128 v[52:55], v219 offset:35840
	ds_read_b128 v[40:43], v219 offset:36864
	ds_read_b128 v[44:47], v219 offset:37888
	ds_read_b128 v[32:35], v219 offset:38912
	ds_read_b128 v[36:39], v219 offset:39936
	s_mov_b32 m0, s27
	s_nop 0
	global_load_lds_dwordx4 v[232:233], off
	s_mov_b32 m0, s28
	s_nop 0
	global_load_lds_dwordx4 v[234:235], off
	s_mov_b32 m0, s31
	s_nop 0
	global_load_lds_dwordx4 v[220:221], off
	v_lshl_add_u64 v[220:221], s[20:21], 0, v[202:203]
	s_mov_b32 m0, s34
	s_and_b64 vcc, exec, s[2:3]
	global_load_lds_dwordx4 v[220:221], off
	s_cbranch_vccnz .LBB0_634
	s_waitcnt vmcnt(24)
	s_cbranch_execnz .LBB0_623
	s_branch .LBB0_635

; #define PG8_STAGE_A(bufoff, gbase, VO, h) do { _Pragma("unroll") for (int _i = 0; _i < 2; ++_i) \
;         __builtin_amdgcn_global_load_lds((const unsigned*)((const char*)(gbase) + (VO)[h][_i]), (LAS unsigned*)(lds + (bufoff) + ldsw + _i * 8192), 16, 0, 0); } while (0)
; #define PG8_BAR __builtin_amdgcn_s_barrier()
;     ...
;         if (ALIGN_EPI) { if (wr == 0) PG8_BAR; }
;         if (ALIGN_EPI && has_next) { if constexpr (GATHER) PG8_STAGE_A(PG8_SA(1, 1), nA + kstep, voffN, 1); else PG8_STAGE_A(PG8_SA(1, 1), nA + kstep, voffA, 1); }
.LBB0_638:
	v_cndmask_b32_e64 v0, 0, 1, s[14:15]
	v_cmp_ne_u32_e64 s[2:3], 1, v0
	s_andn2_b64 vcc, exec, s[14:15]
	s_cbranch_vccnz .LBB0_640
	v_lshl_add_u64 v[2:3], s[8:9], 0, v[196:197]
	v_lshl_add_u64 v[0:1], s[8:9], 0, v[202:203]
	v_lshl_add_u64 v[2:3], v[2:3], 0, s[94:95]
	s_mov_b32 m0, s41
	s_nop 0
	global_load_lds_dwordx4 v[232:233], off
	s_mov_b32 m0, s42
	s_nop 0
	global_load_lds_dwordx4 v[234:235], off
	s_add_i32 m0, s24, 0xc000
	v_lshl_add_u64 v[0:1], v[0:1], 0, s[94:95]
	global_load_lds_dwordx4 v[2:3], off
	s_add_i32 m0, s24, 0xe000
	s_nop 0
	global_load_lds_dwordx4 v[0:1], off

; #define PG8_STAGE_B(bufoff, gbase) do { _Pragma("unroll") for (int _i = 0; _i < 2; ++_i) \
;         __builtin_amdgcn_global_load_lds((const unsigned*)((const char*)(gbase) + voffB[_i]), (LAS unsigned*)(lds + (bufoff) + ldsw + _i * 8192), 16, 0, 0); } while (0)
; #define PG8_STAGE_A(bufoff, gbase, VO, h) do { _Pragma("unroll") for (int _i = 0; _i < 2; ++_i) \
;         __builtin_amdgcn_global_load_lds((const unsigned*)((const char*)(gbase) + (VO)[h][_i]), (LAS unsigned*)(lds + (bufoff) + ldsw + _i * 8192), 16, 0, 0); } while (0)
; #define PG8_WAIT_V(n) asm volatile("s_waitcnt vmcnt(" #n ")" ::: "memory")
; #define PG8_BAR __builtin_amdgcn_s_barrier()
;     ...
;     for (int i = 0; i < 2; ++i) { int R, C; stage_rc(tid * 16 + i * 8192, R, C); const int Rb = (R & ~31) + perm32(R & 31);
;         Rr[i] = R; Cc[i] = C; voffB[i] = nB64 ? (unsigned)(Rb * 64 + ((C * 2) & 63) + ((C * 2) >> 6) * nB64 * 64) : (unsigned)(Rb * ldb + C) * 2u;
;         voffA[0][i] = (unsigned)(R * lda + C) * 2u; voffA[1][i] = (unsigned)((R + HALF) * lda + C) * 2u; voffN[0][i] = voffA[0][i]; voffN[1][i] = voffA[1][i]; }
;     const size_t kstep = (size_t)(BK * 2);
;     const size_t kstepB = kstepB_arg ? kstepB_arg : kstep;
;     const size_t hstepB = nB64 ? (size_t)HALF * 64 : (size_t)HALF * ldb * 2;
;     const unsigned ldsw = (unsigned)wid * 1024u;
;     const int aoff = lds_byte(wr * 64 + fr, fq * 8), boff = lds_byte(wc * 32 + fr, fq * 8);
;     ...
;     PG8_STAGE_B(PG8_SB(0, 0), cB); PG8_STAGE_B(PG8_SB(0, 1), cB + hstepB); PG8_STAGE_A(PG8_SA(0, 0), cA, voffA, 0); PG8_STAGE_A(PG8_SA(0, 1), cA, voffA, 1);
;     if (wr == 1) PG8_BAR;
;     PG8_WAIT_V(2); PG8_BAR;
;     PG8_STAGE_B(PG8_SB(1, 0), cB + kstepB); PG8_STAGE_A(PG8_SA(1, 0), cA + kstep, voffA, 0); PG8_STAGE_B(PG8_SB(1, 1), cB + hstepB + kstepB);
;     PG8_WAIT_V(6); PG8_BAR;
.LBB0_689:
	v_and_b32_e32 v9, 15, v8
	v_readlane_b32 s2, v249, 41
	v_lshrrev_b32_e32 v14, 1, v8
	v_and_b32_e32 v14, 24, v14
	v_or_b32_e32 v207, s2, v9
	v_lshlrev_b32_e32 v15, 6, v207
	v_lshlrev_b32_e32 v16, 1, v14
	s_movk_i32 s2, 0x3c0
	v_lshlrev_b32_e32 v17, 2, v207
	v_and_or_b32 v15, v15, s2, v16
	v_and_b32_e32 v17, 32, v17
	v_readlane_b32 s2, v249, 42
	v_lshlrev_b32_e32 v8, 2, v8
	v_lshl_or_b32 v9, v9, 6, v16
	v_bitop3_b32 v15, v15, s2, v17 bitop3:0xde
	v_and_b32_e32 v8, 32, v8
	v_readlane_b32 s2, v249, 44
	v_mov_b32_e32 v195, v65
	v_mov_b32_e32 v201, v65
	v_bitop3_b32 v16, v9, s2, v8 bitop3:0xde
	s_add_u32 s2, s0, 0x40000
	s_addc_u32 s3, s1, 0
	s_add_i32 s36, s24, 0x18000
	v_mov_b32_e32 v197, v65
	v_lshl_add_u64 v[8:9], s[2:3], 0, v[194:195]
	s_mov_b32 m0, s36
	s_add_i32 s37, s24, 0x1a000
	v_lshl_add_u64 v[10:11], s[6:7], 0, v[196:197]
	v_mov_b32_e32 v203, v65
	s_waitcnt vmcnt(2)
	s_barrier
	global_load_lds_dwordx4 v[8:9], off
	v_lshl_add_u64 v[8:9], s[2:3], 0, v[200:201]
	s_mov_b32 m0, s37
	s_add_i32 s42, s24, 0x8000
	s_add_i32 s43, s24, 0xa000
	v_lshl_add_u64 v[12:13], s[6:7], 0, v[202:203]
	global_load_lds_dwordx4 v[8:9], off
	v_lshl_add_u64 v[8:9], v[10:11], 0, s[94:95]
	s_mov_b32 m0, s42
	s_add_u32 s2, s0, 0x42000
	global_load_lds_dwordx4 v[8:9], off
	v_lshl_add_u64 v[8:9], v[12:13], 0, s[94:95]
	s_mov_b32 m0, s43
	s_addc_u32 s3, s1, 0
	s_add_i32 s44, s24, 0x1c000
	global_load_lds_dwordx4 v[8:9], off
	v_lshl_add_u64 v[232:233], s[2:3], 0, v[194:195]
	s_add_i32 s45, s24, 0x1e000
	v_lshl_add_u64 v[234:235], s[2:3], 0, v[200:201]
	s_movk_i32 s5, 0x600
	v_readlane_b32 s2, v249, 43
	v_lshrrev_b32_e32 v8, 1, v4
	v_mul_lo_u32 v4, v6, s5
	s_movk_i32 s4, 0x6000
	v_or_b32_e32 v206, s2, v14
	v_mad_u64_u32 v[8:9], s[2:3], v8, s4, v[4:5]
	v_or_b32_e32 v4, v8, v5
	v_add_u32_sdwa v4, v4, sext(v7) dst_sel:DWORD dst_unused:UNUSED_PAD src0_sel:DWORD src1_sel:WORD_0
	v_mov_b32_e32 v6, 0x60000
	v_lshl_add_u32 v208, v4, 1, v6
	v_lshrrev_b32_e32 v4, 1, v0
	v_mul_lo_u32 v0, v2, s5
	v_mad_u64_u32 v[4:5], s[2:3], v4, s4, v[0:1]
	s_waitcnt vmcnt(4)
	v_or_b32_e32 v0, v4, v1
	v_add_u32_sdwa v0, v0, sext(v3) dst_sel:DWORD dst_unused:UNUSED_PAD src0_sel:DWORD src1_sel:WORD_0
	v_mov_b32_e32 v199, v65
	v_mov_b32_e32 v205, v65
	v_mov_b32_e32 v209, v65
	v_lshl_add_u32 v210, v0, 1, v6
	v_mov_b32_e32 v211, v65
	s_mov_b32 s46, 0
	s_mov_b64 s[8:9], 0
	v_add_u32_e32 v237, 0, v16
	v_add_u32_e32 v238, 0, v15
	s_mov_b64 s[2:3], s[6:7]
	s_mov_b64 s[4:5], s[0:1]
	s_barrier
	s_branch .LBB0_692

; #define PG8_STAGE_B(bufoff, gbase) do { _Pragma("unroll") for (int _i = 0; _i < 2; ++_i) \
;         __builtin_amdgcn_global_load_lds((const unsigned*)((const char*)(gbase) + voffB[_i]), (LAS unsigned*)(lds + (bufoff) + ldsw + _i * 8192), 16, 0, 0); } while (0)
; #define PG8_STAGE_A(bufoff, gbase, VO, h) do { _Pragma("unroll") for (int _i = 0; _i < 2; ++_i) \
;         __builtin_amdgcn_global_load_lds((const unsigned*)((const char*)(gbase) + (VO)[h][_i]), (LAS unsigned*)(lds + (bufoff) + ldsw + _i * 8192), 16, 0, 0); } while (0)
; #define PG8_WAIT_V(n) asm volatile("s_waitcnt vmcnt(" #n ")" ::: "memory")
; #define PG8_WAIT_L(n) asm volatile("s_waitcnt lgkmcnt(" #n ")" ::: "memory")
; #define PG8_WAIT_VX(rx) do { if (rx) asm volatile("s_waitcnt vmcnt(%0)" :: "n"(8 + Epi::NVM) : "memory"); else asm volatile("s_waitcnt vmcnt(8)" ::: "memory"); } while (0)
; #define PG8_BAR __builtin_amdgcn_s_barrier()
; #define PG8_SCHED __builtin_amdgcn_sched_barrier(0)
;     ...
;             PG8_WAIT_VX(rx); PG8_WAIT_L(0); PG8_BAR; PG8_MMA(0, 0, At, B0); PG8_MMA(0, 1, At, B1); PG8_BAR; PG8_SCHED;
;             PG8_LDA(At, 1, 1); PG8_STAGE_B(PG8_SB(1, 0), b3); PG8_STAGE_B(PG8_SB(1, 1), b3 + hstepB); PG8_STAGE_A(PG8_SA(1, 0), a3, vo2, 0);
;             PG8_WAIT_V(8); PG8_WAIT_L(0); PG8_BAR; PG8_MMA(1, 0, At, B0); PG8_MMA(1, 1, At, B1); PG8_BAR; PG8_SCHED;
.LBB0_699:
	s_waitcnt lgkmcnt(0)
	s_add_u32 s0, s16, 0x40000
	s_addc_u32 s1, s17, 0
	s_barrier
	s_setprio 1
	s_waitcnt lgkmcnt(0)
	v_mfma_scale_f32_16x16x128_f8f6f4 v[190:193], v[24:31], v[56:63], v[190:193], v226, v227 op_sel_hi:[0,0,0]
	v_mfma_scale_f32_16x16x128_f8f6f4 v[186:189], v[16:23], v[56:63], v[186:189], v226, v227 op_sel_hi:[0,0,0]
	v_mfma_scale_f32_16x16x128_f8f6f4 v[174:177], v[24:31], v[48:55], v[174:177], v226, v227 op_sel_hi:[0,0,0]
	v_mfma_scale_f32_16x16x128_f8f6f4 v[170:173], v[16:23], v[48:55], v[170:173], v226, v227 op_sel_hi:[0,0,0]
	v_mfma_scale_f32_16x16x128_f8f6f4 v[158:161], v[24:31], v[40:47], v[158:161], v226, v227 op_sel_hi:[0,0,0]
	v_mfma_scale_f32_16x16x128_f8f6f4 v[154:157], v[16:23], v[40:47], v[154:157], v226, v227 op_sel_hi:[0,0,0]
	v_mfma_scale_f32_16x16x128_f8f6f4 v[142:145], v[24:31], v[32:39], v[142:145], v226, v227 op_sel_hi:[0,0,0]
	v_mfma_scale_f32_16x16x128_f8f6f4 v[138:141], v[16:23], v[32:39], v[138:141], v226, v227 op_sel_hi:[0,0,0]
	s_setprio 0
	s_setprio 1
	v_mfma_scale_f32_16x16x128_f8f6f4 v[182:185], v[8:15], v[56:63], v[182:185], v226, v227 op_sel_hi:[0,0,0]
	v_mfma_scale_f32_16x16x128_f8f6f4 v[178:181], v[0:7], v[56:63], v[178:181], v226, v227 op_sel_hi:[0,0,0]
	v_mfma_scale_f32_16x16x128_f8f6f4 v[166:169], v[8:15], v[48:55], v[166:169], v226, v227 op_sel_hi:[0,0,0]
	v_mfma_scale_f32_16x16x128_f8f6f4 v[162:165], v[0:7], v[48:55], v[162:165], v226, v227 op_sel_hi:[0,0,0]
	v_mfma_scale_f32_16x16x128_f8f6f4 v[150:153], v[8:15], v[40:47], v[150:153], v226, v227 op_sel_hi:[0,0,0]
	v_mfma_scale_f32_16x16x128_f8f6f4 v[146:149], v[0:7], v[40:47], v[146:149], v226, v227 op_sel_hi:[0,0,0]
	v_mfma_scale_f32_16x16x128_f8f6f4 v[134:137], v[8:15], v[32:39], v[134:137], v226, v227 op_sel_hi:[0,0,0]
	v_mfma_scale_f32_16x16x128_f8f6f4 v[130:133], v[0:7], v[32:39], v[130:133], v226, v227 op_sel_hi:[0,0,0]
	s_setprio 0
	s_barrier
	s_mov_b32 m0, s36
	v_lshl_add_u64 v[240:241], s[0:1], 0, v[194:195]
	ds_read_b128 v[32:35], v238 offset:49152
	ds_read_b128 v[36:39], v238 offset:50176
	ds_read_b128 v[40:43], v238 offset:51200
	ds_read_b128 v[44:47], v238 offset:52224
	ds_read_b128 v[48:51], v238 offset:53248
	ds_read_b128 v[52:55], v238 offset:54272
	ds_read_b128 v[56:59], v238 offset:55296
	ds_read_b128 v[60:63], v238 offset:56320
	global_load_lds_dwordx4 v[240:241], off
	v_lshl_add_u64 v[240:241], s[0:1], 0, v[200:201]
	s_add_u32 s0, s16, 0x42000
	s_mov_b32 m0, s37
	s_addc_u32 s1, s17, 0
	global_load_lds_dwordx4 v[240:241], off
	v_lshl_add_u64 v[232:233], s[0:1], 0, v[194:195]
	v_lshl_add_u64 v[218:219], v[218:219], 0, s[94:95]
	v_lshl_add_u64 v[234:235], s[0:1], 0, v[200:201]
	s_mov_b32 m0, s42
	s_nop 0
	global_load_lds_dwordx4 v[218:219], off
	v_lshl_add_u64 v[218:219], v[220:221], 0, s[94:95]
	s_mov_b32 m0, s43
	s_nop 0
	global_load_lds_dwordx4 v[218:219], off
	s_waitcnt vmcnt(6)
	s_waitcnt lgkmcnt(0)
	s_barrier
	s_setprio 1
	s_waitcnt lgkmcnt(0)
	v_mfma_scale_f32_16x16x128_f8f6f4 v[126:129], v[24:31], v[32:39], v[126:129], v226, v227 op_sel_hi:[0,0,0]
	v_mfma_scale_f32_16x16x128_f8f6f4 v[122:125], v[16:23], v[32:39], v[122:125], v226, v227 op_sel_hi:[0,0,0]
	v_mfma_scale_f32_16x16x128_f8f6f4 v[110:113], v[24:31], v[40:47], v[110:113], v226, v227 op_sel_hi:[0,0,0]
	v_mfma_scale_f32_16x16x128_f8f6f4 v[106:109], v[16:23], v[40:47], v[106:109], v226, v227 op_sel_hi:[0,0,0]
	v_mfma_scale_f32_16x16x128_f8f6f4 v[94:97], v[24:31], v[48:55], v[94:97], v226, v227 op_sel_hi:[0,0,0]
	v_mfma_scale_f32_16x16x128_f8f6f4 v[90:93], v[16:23], v[48:55], v[90:93], v226, v227 op_sel_hi:[0,0,0]
	v_mfma_scale_f32_16x16x128_f8f6f4 v[78:81], v[24:31], v[56:63], v[78:81], v226, v227 op_sel_hi:[0,0,0]
	v_mfma_scale_f32_16x16x128_f8f6f4 v[74:77], v[16:23], v[56:63], v[74:77], v226, v227 op_sel_hi:[0,0,0]
	s_setprio 0
	s_setprio 1
	v_mfma_scale_f32_16x16x128_f8f6f4 v[118:121], v[8:15], v[32:39], v[118:121], v226, v227 op_sel_hi:[0,0,0]
	v_mfma_scale_f32_16x16x128_f8f6f4 v[114:117], v[0:7], v[32:39], v[114:117], v226, v227 op_sel_hi:[0,0,0]
	v_mfma_scale_f32_16x16x128_f8f6f4 v[102:105], v[8:15], v[40:47], v[102:105], v226, v227 op_sel_hi:[0,0,0]
	v_mfma_scale_f32_16x16x128_f8f6f4 v[98:101], v[0:7], v[40:47], v[98:101], v226, v227 op_sel_hi:[0,0,0]
	v_mfma_scale_f32_16x16x128_f8f6f4 v[86:89], v[8:15], v[48:55], v[86:89], v226, v227 op_sel_hi:[0,0,0]
	v_mfma_scale_f32_16x16x128_f8f6f4 v[82:85], v[0:7], v[48:55], v[82:85], v226, v227 op_sel_hi:[0,0,0]
	v_mfma_scale_f32_16x16x128_f8f6f4 v[70:73], v[8:15], v[56:63], v[70:73], v226, v227 op_sel_hi:[0,0,0]
	v_mfma_scale_f32_16x16x128_f8f6f4 v[66:69], v[0:7], v[56:63], v[66:69], v226, v227 op_sel_hi:[0,0,0]
	s_setprio 0
	s_barrier
	s_add_i32 s0, s50, 2
	s_add_u32 s31, s31, 0x80000
	s_addc_u32 s49, s49, 0
	s_add_u32 s14, s14, 0x100
	s_addc_u32 s15, s15, 0
	s_cmp_gt_u32 s50, 21
	s_mov_b32 s50, s0
	s_cbranch_scc1 .LBB0_718

; #define PG8_STAGE_B(bufoff, gbase) do { _Pragma("unroll") for (int _i = 0; _i < 2; ++_i) \
;         __builtin_amdgcn_global_load_lds((const unsigned*)((const char*)(gbase) + voffB[_i]), (LAS unsigned*)(lds + (bufoff) + ldsw + _i * 8192), 16, 0, 0); } while (0)
; #define PG8_STAGE_A(bufoff, gbase, VO, h) do { _Pragma("unroll") for (int _i = 0; _i < 2; ++_i) \
;         __builtin_amdgcn_global_load_lds((const unsigned*)((const char*)(gbase) + (VO)[h][_i]), (LAS unsigned*)(lds + (bufoff) + ldsw + _i * 8192), 16, 0, 0); } while (0)
; #define PG8_WAIT_L(n) asm volatile("s_waitcnt lgkmcnt(" #n ")" ::: "memory")
; #define PG8_WAIT_VX(rx) do { if (rx) asm volatile("s_waitcnt vmcnt(%0)" :: "n"(8 + Epi::NVM) : "memory"); else asm volatile("s_waitcnt vmcnt(8)" ::: "memory"); } while (0)
; #define PG8_BAR __builtin_amdgcn_s_barrier()
; #define PG8_SCHED __builtin_amdgcn_sched_barrier(0)
;     ...
;             PG8_LDB(B0, 0, 0); PG8_LDB(B1, 0, 1); PG8_SCHED; PG8_LDA(At, 0, 0); if (!rx) PG8_STAGE_A(PG8_SA(1, 1), a1, voffA, 1);
;             PG8_WAIT_VX(rx); PG8_WAIT_L(0); PG8_BAR; PG8_MMA(0, 0, At, B0); PG8_MMA(0, 1, At, B1); PG8_BAR; PG8_SCHED;
;             PG8_LDA(At, 0, 1); PG8_STAGE_B(PG8_SB(0, 0), b2); PG8_STAGE_B(PG8_SB(0, 1), b2 + hstepB); PG8_STAGE_A(PG8_SA(0, 0), a2, vo2, 0);
.LBB0_708:
	s_mov_b32 m0, s44
	s_nop 0
	global_load_lds_dwordx4 v[232:233], off
	s_mov_b32 m0, s45
	s_nop 0
	global_load_lds_dwordx4 v[234:235], off
	v_lshl_add_u64 v[218:219], v[216:217], 0, s[14:15]
	s_add_i32 m0, s24, 0xc000
	s_nop 0
	global_load_lds_dwordx4 v[218:219], off
	v_lshl_add_u64 v[218:219], v[214:215], 0, s[14:15]
	s_add_i32 m0, s24, 0xe000
	s_nop 0
	global_load_lds_dwordx4 v[218:219], off
	s_waitcnt vmcnt(8)
.LBB0_709:
	s_add_u32 s0, s6, s14
	s_addc_u32 s1, s7, s15
	s_add_u32 s0, s0, 0x100
	s_addc_u32 s1, s1, 0
	s_waitcnt lgkmcnt(0)
	s_cmpk_eq_i32 s14, 0xb00
	s_cselect_b32 s19, s3, s1
	s_cselect_b32 s18, s2, s0
	s_cselect_b32 s17, s5, s49
	s_cselect_b32 s16, s4, s31
	s_barrier
	s_setprio 1
	s_waitcnt lgkmcnt(0)
	v_mfma_scale_f32_16x16x128_f8f6f4 v[190:193], v[24:31], v[56:63], v[190:193], v226, v227 op_sel_hi:[0,0,0]
	v_mfma_scale_f32_16x16x128_f8f6f4 v[186:189], v[16:23], v[56:63], v[186:189], v226, v227 op_sel_hi:[0,0,0]
	v_mfma_scale_f32_16x16x128_f8f6f4 v[174:177], v[24:31], v[48:55], v[174:177], v226, v227 op_sel_hi:[0,0,0]
	v_mfma_scale_f32_16x16x128_f8f6f4 v[170:173], v[16:23], v[48:55], v[170:173], v226, v227 op_sel_hi:[0,0,0]
	v_mfma_scale_f32_16x16x128_f8f6f4 v[158:161], v[24:31], v[40:47], v[158:161], v226, v227 op_sel_hi:[0,0,0]
	v_mfma_scale_f32_16x16x128_f8f6f4 v[154:157], v[16:23], v[40:47], v[154:157], v226, v227 op_sel_hi:[0,0,0]
	v_mfma_scale_f32_16x16x128_f8f6f4 v[142:145], v[24:31], v[32:39], v[142:145], v226, v227 op_sel_hi:[0,0,0]
	v_mfma_scale_f32_16x16x128_f8f6f4 v[138:141], v[16:23], v[32:39], v[138:141], v226, v227 op_sel_hi:[0,0,0]
	s_setprio 0
	s_setprio 1
	v_mfma_scale_f32_16x16x128_f8f6f4 v[182:185], v[8:15], v[56:63], v[182:185], v226, v227 op_sel_hi:[0,0,0]
	v_mfma_scale_f32_16x16x128_f8f6f4 v[178:181], v[0:7], v[56:63], v[178:181], v226, v227 op_sel_hi:[0,0,0]
	v_mfma_scale_f32_16x16x128_f8f6f4 v[166:169], v[8:15], v[48:55], v[166:169], v226, v227 op_sel_hi:[0,0,0]
	v_mfma_scale_f32_16x16x128_f8f6f4 v[162:165], v[0:7], v[48:55], v[162:165], v226, v227 op_sel_hi:[0,0,0]
	v_mfma_scale_f32_16x16x128_f8f6f4 v[150:153], v[8:15], v[40:47], v[150:153], v226, v227 op_sel_hi:[0,0,0]
	v_mfma_scale_f32_16x16x128_f8f6f4 v[146:149], v[0:7], v[40:47], v[146:149], v226, v227 op_sel_hi:[0,0,0]
	v_mfma_scale_f32_16x16x128_f8f6f4 v[134:137], v[8:15], v[32:39], v[134:137], v226, v227 op_sel_hi:[0,0,0]
	v_mfma_scale_f32_16x16x128_f8f6f4 v[130:133], v[0:7], v[32:39], v[130:133], v226, v227 op_sel_hi:[0,0,0]
	s_setprio 0
	s_barrier
	s_mov_b32 m0, s25
	v_lshl_add_u64 v[218:219], s[16:17], 0, v[194:195]
	s_add_u32 s0, s16, 0x2000
	ds_read_b128 v[56:59], v238 offset:16384
	ds_read_b128 v[60:63], v238 offset:17408
	ds_read_b128 v[48:51], v238 offset:18432
	ds_read_b128 v[52:55], v238 offset:19456
	ds_read_b128 v[40:43], v238 offset:20480
	ds_read_b128 v[44:47], v238 offset:21504
	ds_read_b128 v[32:35], v238 offset:22528
	ds_read_b128 v[36:39], v238 offset:23552
	global_load_lds_dwordx4 v[218:219], off
	v_lshl_add_u64 v[218:219], s[16:17], 0, v[200:201]
	s_mov_b32 m0, s26
	s_addc_u32 s1, s17, 0
	global_load_lds_dwordx4 v[218:219], off
	v_lshl_add_u64 v[232:233], s[0:1], 0, v[194:195]
	v_lshl_add_u64 v[220:221], s[18:19], 0, v[202:203]
	v_lshl_add_u64 v[234:235], s[0:1], 0, v[200:201]
	v_cndmask_b32_e64 v64, 0, 1, s[20:21]
	v_lshl_add_u64 v[218:219], s[18:19], 0, v[196:197]
	s_mov_b32 m0, s24
	v_cmp_ne_u32_e64 s[0:1], 1, v64
	global_load_lds_dwordx4 v[218:219], off
	s_mov_b32 m0, s29
	s_andn2_b64 vcc, exec, s[20:21]
	global_load_lds_dwordx4 v[220:221], off
	s_cbranch_vccnz .LBB0_715
	s_waitcnt vmcnt(22)
	s_cbranch_execnz .LBB0_712

; #define PG8_STAGE_A(bufoff, gbase, VO, h) do { _Pragma("unroll") for (int _i = 0; _i < 2; ++_i) \
;         __builtin_amdgcn_global_load_lds((const unsigned*)((const char*)(gbase) + (VO)[h][_i]), (LAS unsigned*)(lds + (bufoff) + ldsw + _i * 8192), 16, 0, 0); } while (0)
; #define PG8_WAIT_L(n) asm volatile("s_waitcnt lgkmcnt(" #n ")" ::: "memory")
; #define PG8_WAIT_VX(rx) do { if (rx) asm volatile("s_waitcnt vmcnt(%0)" :: "n"(8 + Epi::NVM) : "memory"); else asm volatile("s_waitcnt vmcnt(8)" ::: "memory"); } while (0)
; #define PG8_BAR __builtin_amdgcn_s_barrier()
; #define PG8_SCHED __builtin_amdgcn_sched_barrier(0)
;     ...
;             PG8_WAIT_VX(rx); PG8_WAIT_L(0); PG8_BAR; PG8_MMA(1, 0, At, B0); PG8_MMA(1, 1, At, B1); PG8_BAR; PG8_SCHED;
;             PG8_LDB(B0, 1, 0); PG8_LDB(B1, 1, 1); PG8_SCHED; PG8_LDA(At, 1, 0); PG8_STAGE_A(PG8_SA(0, 1), a2, vo2, 1);
.LBB0_712:
	s_waitcnt lgkmcnt(0)
	s_barrier
	s_setprio 1
	s_waitcnt lgkmcnt(0)
	v_mfma_scale_f32_16x16x128_f8f6f4 v[126:129], v[24:31], v[56:63], v[126:129], v226, v227 op_sel_hi:[0,0,0]
	v_mfma_scale_f32_16x16x128_f8f6f4 v[122:125], v[16:23], v[56:63], v[122:125], v226, v227 op_sel_hi:[0,0,0]
	v_mfma_scale_f32_16x16x128_f8f6f4 v[110:113], v[24:31], v[48:55], v[110:113], v226, v227 op_sel_hi:[0,0,0]
	v_mfma_scale_f32_16x16x128_f8f6f4 v[106:109], v[16:23], v[48:55], v[106:109], v226, v227 op_sel_hi:[0,0,0]
	v_mfma_scale_f32_16x16x128_f8f6f4 v[94:97], v[24:31], v[40:47], v[94:97], v226, v227 op_sel_hi:[0,0,0]
	v_mfma_scale_f32_16x16x128_f8f6f4 v[90:93], v[16:23], v[40:47], v[90:93], v226, v227 op_sel_hi:[0,0,0]
	v_mfma_scale_f32_16x16x128_f8f6f4 v[78:81], v[24:31], v[32:39], v[78:81], v226, v227 op_sel_hi:[0,0,0]
	v_mfma_scale_f32_16x16x128_f8f6f4 v[74:77], v[16:23], v[32:39], v[74:77], v226, v227 op_sel_hi:[0,0,0]
	s_setprio 0
	s_setprio 1
	v_mfma_scale_f32_16x16x128_f8f6f4 v[118:121], v[8:15], v[56:63], v[118:121], v226, v227 op_sel_hi:[0,0,0]
	v_mfma_scale_f32_16x16x128_f8f6f4 v[114:117], v[0:7], v[56:63], v[114:117], v226, v227 op_sel_hi:[0,0,0]
	v_mfma_scale_f32_16x16x128_f8f6f4 v[102:105], v[8:15], v[48:55], v[102:105], v226, v227 op_sel_hi:[0,0,0]
	v_mfma_scale_f32_16x16x128_f8f6f4 v[98:101], v[0:7], v[48:55], v[98:101], v226, v227 op_sel_hi:[0,0,0]
	v_mfma_scale_f32_16x16x128_f8f6f4 v[86:89], v[8:15], v[40:47], v[86:89], v226, v227 op_sel_hi:[0,0,0]
	v_mfma_scale_f32_16x16x128_f8f6f4 v[82:85], v[0:7], v[40:47], v[82:85], v226, v227 op_sel_hi:[0,0,0]
	v_mfma_scale_f32_16x16x128_f8f6f4 v[70:73], v[8:15], v[32:39], v[70:73], v226, v227 op_sel_hi:[0,0,0]
	v_mfma_scale_f32_16x16x128_f8f6f4 v[66:69], v[0:7], v[32:39], v[66:69], v226, v227 op_sel_hi:[0,0,0]
	s_setprio 0
	s_barrier
	v_add_u32_e32 v0, 0x18000, v237
	v_add_u32_e32 v4, 0x1c000, v237
	ds_read_b128 v[24:27], v0
	ds_read_b128 v[28:31], v0 offset:1024
	ds_read_b128 v[16:19], v0 offset:2048
	ds_read_b128 v[20:23], v0 offset:3072
	ds_read_b128 v[8:11], v4
	ds_read_b128 v[12:15], v4 offset:1024
	ds_read_b128 v[0:3], v4 offset:2048
	ds_read_b128 v[4:7], v4 offset:3072
	s_mov_b32 m0, s34
	v_lshl_add_u64 v[240:241], s[18:19], 0, v[198:199]
	ds_read_b128 v[56:59], v238 offset:32768
	ds_read_b128 v[60:63], v238 offset:33792
	ds_read_b128 v[48:51], v238 offset:34816
	ds_read_b128 v[52:55], v238 offset:35840
	ds_read_b128 v[40:43], v238 offset:36864
	ds_read_b128 v[44:47], v238 offset:37888
	ds_read_b128 v[32:35], v238 offset:38912
	ds_read_b128 v[36:39], v238 offset:39936
	s_mov_b32 m0, s27
	s_nop 0
	global_load_lds_dwordx4 v[232:233], off
	s_mov_b32 m0, s28
	s_nop 0
	global_load_lds_dwordx4 v[234:235], off
	s_mov_b32 m0, s34
	s_nop 0
	global_load_lds_dwordx4 v[240:241], off
	v_lshl_add_u64 v[240:241], s[18:19], 0, v[204:205]
	s_mov_b32 m0, s35
	s_and_b64 vcc, exec, s[0:1]
	global_load_lds_dwordx4 v[240:241], off
	s_cbranch_vccnz .LBB0_716
	s_waitcnt vmcnt(24)
	s_cbranch_execnz .LBB0_699
	s_branch .LBB0_717

; #define PG8_STAGE_A(bufoff, gbase, VO, h) do { _Pragma("unroll") for (int _i = 0; _i < 2; ++_i) \
;         __builtin_amdgcn_global_load_lds((const unsigned*)((const char*)(gbase) + (VO)[h][_i]), (LAS unsigned*)(lds + (bufoff) + ldsw + _i * 8192), 16, 0, 0); } while (0)
; #define PG8_BAR __builtin_amdgcn_s_barrier()
;     ...
;         if (ALIGN_EPI) { if (wr == 0) PG8_BAR; }
;         if (ALIGN_EPI && has_next) { if constexpr (GATHER) PG8_STAGE_A(PG8_SA(1, 1), nA + kstep, voffN, 1); else PG8_STAGE_A(PG8_SA(1, 1), nA + kstep, voffA, 1); }
.LBB0_720:
	v_cndmask_b32_e64 v0, 0, 1, s[10:11]
	v_cmp_ne_u32_e64 s[0:1], 1, v0
	s_andn2_b64 vcc, exec, s[10:11]
	s_cbranch_vccnz .LBB0_722
	v_lshl_add_u64 v[2:3], s[2:3], 0, v[198:199]
	v_lshl_add_u64 v[0:1], s[2:3], 0, v[204:205]
	v_lshl_add_u64 v[2:3], v[2:3], 0, s[94:95]
	s_mov_b32 m0, s44
	s_nop 0
	global_load_lds_dwordx4 v[232:233], off
	s_mov_b32 m0, s45
	s_nop 0
	global_load_lds_dwordx4 v[234:235], off
	s_add_i32 m0, s24, 0xc000
	v_lshl_add_u64 v[0:1], v[0:1], 0, s[94:95]
	global_load_lds_dwordx4 v[2:3], off
	s_add_i32 m0, s24, 0xe000
	s_nop 0
	global_load_lds_dwordx4 v[0:1], off

; #define PG8_STAGE_B(bufoff, gbase) do { _Pragma("unroll") for (int _i = 0; _i < 2; ++_i) \
;         __builtin_amdgcn_global_load_lds((const unsigned*)((const char*)(gbase) + voffB[_i]), (LAS unsigned*)(lds + (bufoff) + ldsw + _i * 8192), 16, 0, 0); } while (0)
; #define PG8_STAGE_A(bufoff, gbase, VO, h) do { _Pragma("unroll") for (int _i = 0; _i < 2; ++_i) \
;         __builtin_amdgcn_global_load_lds((const unsigned*)((const char*)(gbase) + (VO)[h][_i]), (LAS unsigned*)(lds + (bufoff) + ldsw + _i * 8192), 16, 0, 0); } while (0)
; #define PG8_WAIT_V(n) asm volatile("s_waitcnt vmcnt(" #n ")" ::: "memory")
; #define PG8_BAR __builtin_amdgcn_s_barrier()
;     ...
;     for (int i = 0; i < 2; ++i) { int R, C; stage_rc(tid * 16 + i * 8192, R, C); const int Rb = (R & ~31) + perm32(R & 31);
;         Rr[i] = R; Cc[i] = C; voffB[i] = nB64 ? (unsigned)(Rb * 64 + ((C * 2) & 63) + ((C * 2) >> 6) * nB64 * 64) : (unsigned)(Rb * ldb + C) * 2u;
;         voffA[0][i] = (unsigned)(R * lda + C) * 2u; voffA[1][i] = (unsigned)((R + HALF) * lda + C) * 2u; voffN[0][i] = voffA[0][i]; voffN[1][i] = voffA[1][i]; }
;     const size_t kstep = (size_t)(BK * 2);
;     const size_t kstepB = kstepB_arg ? kstepB_arg : kstep;
;     const size_t hstepB = nB64 ? (size_t)HALF * 64 : (size_t)HALF * ldb * 2;
;     const unsigned ldsw = (unsigned)wid * 1024u;
;     const int aoff = lds_byte(wr * 64 + fr, fq * 8), boff = lds_byte(wc * 32 + fr, fq * 8);
;     ...
;     PG8_STAGE_B(PG8_SB(0, 0), cB); PG8_STAGE_B(PG8_SB(0, 1), cB + hstepB); PG8_STAGE_A(PG8_SA(0, 0), cA, voffA, 0); PG8_STAGE_A(PG8_SA(0, 1), cA, voffA, 1);
;     if (wr == 1) PG8_BAR;
;     PG8_WAIT_V(2); PG8_BAR;
;     PG8_STAGE_B(PG8_SB(1, 0), cB + kstepB); PG8_STAGE_A(PG8_SA(1, 0), cA + kstep, voffA, 0); PG8_STAGE_B(PG8_SB(1, 1), cB + hstepB + kstepB);
;     PG8_WAIT_V(6); PG8_BAR;
.LBB0_784:
	v_and_b32_e32 v9, 15, v8
	v_readlane_b32 s6, v249, 41
	v_lshrrev_b32_e32 v14, 1, v8
	v_and_b32_e32 v14, 24, v14
	v_or_b32_e32 v218, s6, v9
	v_lshlrev_b32_e32 v15, 6, v218
	v_lshlrev_b32_e32 v16, 1, v14
	s_movk_i32 s6, 0x3c0
	v_lshlrev_b32_e32 v17, 2, v218
	v_and_or_b32 v15, v15, s6, v16
	v_and_b32_e32 v17, 32, v17
	v_readlane_b32 s6, v249, 42
	v_lshlrev_b32_e32 v8, 2, v8
	v_lshl_or_b32 v9, v9, 6, v16
	v_bitop3_b32 v15, v15, s6, v17 bitop3:0xde
	v_and_b32_e32 v8, 32, v8
	v_readlane_b32 s6, v249, 44
	v_mov_b32_e32 v195, v65
	v_mov_b32_e32 v201, v65
	v_bitop3_b32 v16, v9, s6, v8 bitop3:0xde
	s_add_u32 s6, s2, 0x40000
	s_addc_u32 s7, s3, 0
	s_add_i32 s35, s24, 0x18000
	v_mov_b32_e32 v197, v65
	v_lshl_add_u64 v[8:9], s[6:7], 0, v[194:195]
	s_mov_b32 m0, s35
	s_add_i32 s36, s24, 0x1a000
	v_lshl_add_u64 v[10:11], s[4:5], 0, v[196:197]
	v_mov_b32_e32 v203, v65
	s_waitcnt vmcnt(2)
	s_barrier
	global_load_lds_dwordx4 v[8:9], off
	v_lshl_add_u64 v[8:9], s[6:7], 0, v[200:201]
	s_mov_b32 m0, s36
	s_add_i32 s37, s24, 0x8000
	s_add_i32 s40, s24, 0xa000
	v_lshl_add_u64 v[12:13], s[4:5], 0, v[202:203]
	global_load_lds_dwordx4 v[8:9], off
	v_lshl_add_u64 v[8:9], v[10:11], 0, s[94:95]
	s_mov_b32 m0, s37
	s_add_u32 s6, s2, 0x42000
	global_load_lds_dwordx4 v[8:9], off
	v_lshl_add_u64 v[8:9], v[12:13], 0, s[94:95]
	s_mov_b32 m0, s40
	s_addc_u32 s7, s3, 0
	s_add_i32 s41, s24, 0x1c000
	global_load_lds_dwordx4 v[8:9], off
	v_lshl_add_u64 v[232:233], s[6:7], 0, v[194:195]
	s_add_i32 s42, s24, 0x1e000
	v_lshl_add_u64 v[234:235], s[6:7], 0, v[200:201]
	v_lshlrev_b32_e32 v4, 13, v4
	v_lshlrev_b32_e32 v0, 13, v0
	v_and_b32_e32 v4, 0x7fffc000, v4
	v_and_b32_e32 v0, 0x7fffc000, v0
	v_lshl_add_u32 v4, v5, 10, v4
	v_lshl_add_u32 v0, v1, 10, v0
	s_waitcnt vmcnt(4)
	v_readlane_b32 s6, v249, 43
	v_or_b32_e32 v4, v4, v6
	v_or_b32_e32 v0, v0, v2
	v_or_b32_e32 v8, s6, v14
	v_add_u32_sdwa v4, v4, sext(v7) dst_sel:DWORD dst_unused:UNUSED_PAD src0_sel:DWORD src1_sel:WORD_0
	v_mov_b32_e32 v5, 0x40000
	v_add_u32_sdwa v0, v0, sext(v3) dst_sel:DWORD dst_unused:UNUSED_PAD src0_sel:DWORD src1_sel:WORD_0
	v_mov_b32_e32 v199, v65
	v_mov_b32_e32 v205, v65
	v_lshl_add_u32 v206, v4, 1, v5
	v_mov_b32_e32 v207, v65
	v_lshl_add_u32 v208, v0, 1, v5
	v_mov_b32_e32 v209, v65
	s_mov_b32 s43, 0
	s_mov_b64 s[10:11], 0
	v_lshlrev_b32_e32 v64, 1, v8
	v_add_u32_e32 v219, 0, v16
	v_add_u32_e32 v220, 0, v15
	s_mov_b64 s[6:7], s[4:5]
	s_mov_b64 s[8:9], s[2:3]
	s_barrier
	s_branch .LBB0_787

; #define PG8_STAGE_B(bufoff, gbase) do { _Pragma("unroll") for (int _i = 0; _i < 2; ++_i) \
;         __builtin_amdgcn_global_load_lds((const unsigned*)((const char*)(gbase) + voffB[_i]), (LAS unsigned*)(lds + (bufoff) + ldsw + _i * 8192), 16, 0, 0); } while (0)
; #define PG8_STAGE_A(bufoff, gbase, VO, h) do { _Pragma("unroll") for (int _i = 0; _i < 2; ++_i) \
;         __builtin_amdgcn_global_load_lds((const unsigned*)((const char*)(gbase) + (VO)[h][_i]), (LAS unsigned*)(lds + (bufoff) + ldsw + _i * 8192), 16, 0, 0); } while (0)
; #define PG8_WAIT_V(n) asm volatile("s_waitcnt vmcnt(" #n ")" ::: "memory")
; #define PG8_WAIT_L(n) asm volatile("s_waitcnt lgkmcnt(" #n ")" ::: "memory")
; #define PG8_WAIT_VX(rx) do { if (rx) asm volatile("s_waitcnt vmcnt(%0)" :: "n"(8 + Epi::NVM) : "memory"); else asm volatile("s_waitcnt vmcnt(8)" ::: "memory"); } while (0)
; #define PG8_BAR __builtin_amdgcn_s_barrier()
; #define PG8_SCHED __builtin_amdgcn_sched_barrier(0)
;     ...
;             PG8_WAIT_VX(rx); PG8_WAIT_L(0); PG8_BAR; PG8_MMA(0, 0, At, B0); PG8_MMA(0, 1, At, B1); PG8_BAR; PG8_SCHED;
;             PG8_LDA(At, 1, 1); PG8_STAGE_B(PG8_SB(1, 0), b3); PG8_STAGE_B(PG8_SB(1, 1), b3 + hstepB); PG8_STAGE_A(PG8_SA(1, 0), a3, vo2, 0);
;             PG8_WAIT_V(8); PG8_WAIT_L(0); PG8_BAR; PG8_MMA(1, 0, At, B0); PG8_MMA(1, 1, At, B1); PG8_BAR; PG8_SCHED;
.LBB0_794:
	s_waitcnt lgkmcnt(0)
	s_add_u32 s2, s16, 0x40000
	s_addc_u32 s3, s17, 0
	s_barrier
	s_setprio 1
	s_waitcnt lgkmcnt(0)
	v_mfma_scale_f32_16x16x128_f8f6f4 v[190:193], v[24:31], v[56:63], v[190:193], v226, v227 op_sel_hi:[0,0,0]
	v_mfma_scale_f32_16x16x128_f8f6f4 v[186:189], v[16:23], v[56:63], v[186:189], v226, v227 op_sel_hi:[0,0,0]
	v_mfma_scale_f32_16x16x128_f8f6f4 v[182:185], v[24:31], v[48:55], v[182:185], v226, v227 op_sel_hi:[0,0,0]
	v_mfma_scale_f32_16x16x128_f8f6f4 v[174:177], v[16:23], v[48:55], v[174:177], v226, v227 op_sel_hi:[0,0,0]
	v_mfma_scale_f32_16x16x128_f8f6f4 v[166:169], v[24:31], v[40:47], v[166:169], v226, v227 op_sel_hi:[0,0,0]
	v_mfma_scale_f32_16x16x128_f8f6f4 v[158:161], v[16:23], v[40:47], v[158:161], v226, v227 op_sel_hi:[0,0,0]
	v_mfma_scale_f32_16x16x128_f8f6f4 v[150:153], v[24:31], v[32:39], v[150:153], v226, v227 op_sel_hi:[0,0,0]
	v_mfma_scale_f32_16x16x128_f8f6f4 v[142:145], v[16:23], v[32:39], v[142:145], v226, v227 op_sel_hi:[0,0,0]
	s_setprio 0
	s_setprio 1
	v_mfma_scale_f32_16x16x128_f8f6f4 v[178:181], v[8:15], v[56:63], v[178:181], v226, v227 op_sel_hi:[0,0,0]
	v_mfma_scale_f32_16x16x128_f8f6f4 v[170:173], v[0:7], v[56:63], v[170:173], v226, v227 op_sel_hi:[0,0,0]
	v_mfma_scale_f32_16x16x128_f8f6f4 v[162:165], v[8:15], v[48:55], v[162:165], v226, v227 op_sel_hi:[0,0,0]
	v_mfma_scale_f32_16x16x128_f8f6f4 v[154:157], v[0:7], v[48:55], v[154:157], v226, v227 op_sel_hi:[0,0,0]
	v_mfma_scale_f32_16x16x128_f8f6f4 v[146:149], v[8:15], v[40:47], v[146:149], v226, v227 op_sel_hi:[0,0,0]
	v_mfma_scale_f32_16x16x128_f8f6f4 v[138:141], v[0:7], v[40:47], v[138:141], v226, v227 op_sel_hi:[0,0,0]
	v_mfma_scale_f32_16x16x128_f8f6f4 v[134:137], v[8:15], v[32:39], v[134:137], v226, v227 op_sel_hi:[0,0,0]
	v_mfma_scale_f32_16x16x128_f8f6f4 v[130:133], v[0:7], v[32:39], v[130:133], v226, v227 op_sel_hi:[0,0,0]
	s_setprio 0
	s_barrier
	s_mov_b32 m0, s35
	v_lshl_add_u64 v[238:239], s[2:3], 0, v[194:195]
	ds_read_b128 v[32:35], v220 offset:49152
	ds_read_b128 v[36:39], v220 offset:50176
	ds_read_b128 v[40:43], v220 offset:51200
	ds_read_b128 v[44:47], v220 offset:52224
	ds_read_b128 v[48:51], v220 offset:53248
	ds_read_b128 v[52:55], v220 offset:54272
	ds_read_b128 v[56:59], v220 offset:55296
	ds_read_b128 v[60:63], v220 offset:56320
	global_load_lds_dwordx4 v[238:239], off
	v_lshl_add_u64 v[238:239], s[2:3], 0, v[200:201]
	s_add_u32 s2, s16, 0x42000
	s_mov_b32 m0, s36
	s_addc_u32 s3, s17, 0
	global_load_lds_dwordx4 v[238:239], off
	v_lshl_add_u64 v[232:233], s[2:3], 0, v[194:195]
	v_lshl_add_u64 v[214:215], v[214:215], 0, s[94:95]
	v_lshl_add_u64 v[234:235], s[2:3], 0, v[200:201]
	s_mov_b32 m0, s37
	s_nop 0
	global_load_lds_dwordx4 v[214:215], off
	v_lshl_add_u64 v[214:215], v[216:217], 0, s[94:95]
	s_mov_b32 m0, s40
	s_nop 0
	global_load_lds_dwordx4 v[214:215], off
	s_waitcnt vmcnt(6)
	s_waitcnt lgkmcnt(0)
	s_barrier
	s_setprio 1
	s_waitcnt lgkmcnt(0)
	v_mfma_scale_f32_16x16x128_f8f6f4 v[126:129], v[24:31], v[32:39], v[126:129], v226, v227 op_sel_hi:[0,0,0]
	v_mfma_scale_f32_16x16x128_f8f6f4 v[122:125], v[16:23], v[32:39], v[122:125], v226, v227 op_sel_hi:[0,0,0]
	v_mfma_scale_f32_16x16x128_f8f6f4 v[110:113], v[24:31], v[40:47], v[110:113], v226, v227 op_sel_hi:[0,0,0]
	v_mfma_scale_f32_16x16x128_f8f6f4 v[102:105], v[16:23], v[40:47], v[102:105], v226, v227 op_sel_hi:[0,0,0]
	v_mfma_scale_f32_16x16x128_f8f6f4 v[86:89], v[24:31], v[48:55], v[86:89], v226, v227 op_sel_hi:[0,0,0]
	v_mfma_scale_f32_16x16x128_f8f6f4 v[78:81], v[16:23], v[48:55], v[78:81], v226, v227 op_sel_hi:[0,0,0]
	v_mfma_scale_f32_16x16x128_f8f6f4 v[70:73], v[24:31], v[56:63], v[70:73], v226, v227 op_sel_hi:[0,0,0]
	v_mfma_scale_f32_16x16x128_f8f6f4 v[66:69], v[16:23], v[56:63], v[66:69], v226, v227 op_sel_hi:[0,0,0]
	s_setprio 0
	s_setprio 1
	v_mfma_scale_f32_16x16x128_f8f6f4 v[106:109], v[8:15], v[32:39], v[106:109], v226, v227 op_sel_hi:[0,0,0]
	v_mfma_scale_f32_16x16x128_f8f6f4 v[98:101], v[0:7], v[32:39], v[98:101], v226, v227 op_sel_hi:[0,0,0]
	v_mfma_scale_f32_16x16x128_f8f6f4 v[82:85], v[8:15], v[40:47], v[82:85], v226, v227 op_sel_hi:[0,0,0]
	v_mfma_scale_f32_16x16x128_f8f6f4 v[74:77], v[0:7], v[40:47], v[74:77], v226, v227 op_sel_hi:[0,0,0]
	v_mfma_scale_f32_16x16x128_f8f6f4 v[118:121], v[8:15], v[48:55], v[118:121], v226, v227 op_sel_hi:[0,0,0]
	v_mfma_scale_f32_16x16x128_f8f6f4 v[114:117], v[0:7], v[48:55], v[114:117], v226, v227 op_sel_hi:[0,0,0]
	v_mfma_scale_f32_16x16x128_f8f6f4 v[94:97], v[8:15], v[56:63], v[94:97], v226, v227 op_sel_hi:[0,0,0]
	v_mfma_scale_f32_16x16x128_f8f6f4 v[90:93], v[0:7], v[56:63], v[90:93], v226, v227 op_sel_hi:[0,0,0]
	s_setprio 0
	s_barrier
	s_add_i32 s50, s50, 2
	s_add_u32 s48, s48, 0x80000
	s_addc_u32 s49, s49, 0
	s_add_u32 s14, s14, 0x100
	s_addc_u32 s15, s15, 0
	s_cmp_gt_u32 s50, 13
	s_cbranch_scc1 .LBB0_807

; #define PG8_STAGE_B(bufoff, gbase) do { _Pragma("unroll") for (int _i = 0; _i < 2; ++_i) \
;         __builtin_amdgcn_global_load_lds((const unsigned*)((const char*)(gbase) + voffB[_i]), (LAS unsigned*)(lds + (bufoff) + ldsw + _i * 8192), 16, 0, 0); } while (0)
; #define PG8_STAGE_A(bufoff, gbase, VO, h) do { _Pragma("unroll") for (int _i = 0; _i < 2; ++_i) \
;         __builtin_amdgcn_global_load_lds((const unsigned*)((const char*)(gbase) + (VO)[h][_i]), (LAS unsigned*)(lds + (bufoff) + ldsw + _i * 8192), 16, 0, 0); } while (0)
; #define PG8_WAIT_L(n) asm volatile("s_waitcnt lgkmcnt(" #n ")" ::: "memory")
; #define PG8_WAIT_VX(rx) do { if (rx) asm volatile("s_waitcnt vmcnt(%0)" :: "n"(8 + Epi::NVM) : "memory"); else asm volatile("s_waitcnt vmcnt(8)" ::: "memory"); } while (0)
; #define PG8_BAR __builtin_amdgcn_s_barrier()
; #define PG8_SCHED __builtin_amdgcn_sched_barrier(0)
;     ...
;             PG8_LDB(B0, 0, 0); PG8_LDB(B1, 0, 1); PG8_SCHED; PG8_LDA(At, 0, 0); if (!rx) PG8_STAGE_A(PG8_SA(1, 1), a1, voffA, 1);
;             PG8_WAIT_VX(rx); PG8_WAIT_L(0); PG8_BAR; PG8_MMA(0, 0, At, B0); PG8_MMA(0, 1, At, B1); PG8_BAR; PG8_SCHED;
;             PG8_LDA(At, 0, 1); PG8_STAGE_B(PG8_SB(0, 0), b2); PG8_STAGE_B(PG8_SB(0, 1), b2 + hstepB); PG8_STAGE_A(PG8_SA(0, 0), a2, vo2, 0);
.LBB0_797:
	s_mov_b32 m0, s41
	s_nop 0
	global_load_lds_dwordx4 v[232:233], off
	s_mov_b32 m0, s42
	s_nop 0
	global_load_lds_dwordx4 v[234:235], off
	v_lshl_add_u64 v[214:215], v[212:213], 0, s[14:15]
	s_add_i32 m0, s24, 0xc000
	s_nop 0
	global_load_lds_dwordx4 v[214:215], off
	v_lshl_add_u64 v[214:215], v[210:211], 0, s[14:15]
	s_add_i32 m0, s24, 0xe000
	s_nop 0
	global_load_lds_dwordx4 v[214:215], off
	s_waitcnt vmcnt(8)
.LBB0_798:
	s_add_u32 s2, s4, s14
	s_addc_u32 s3, s5, s15
	s_add_u32 s2, s2, 0x100
	s_addc_u32 s3, s3, 0
	s_waitcnt lgkmcnt(0)
	s_cmpk_eq_i32 s14, 0x700
	s_cselect_b32 s19, s7, s3
	s_cselect_b32 s18, s6, s2
	s_cselect_b32 s17, s9, s49
	s_cselect_b32 s16, s8, s48
	s_barrier
	s_setprio 1
	s_waitcnt lgkmcnt(0)
	v_mfma_scale_f32_16x16x128_f8f6f4 v[190:193], v[24:31], v[56:63], v[190:193], v226, v227 op_sel_hi:[0,0,0]
	v_mfma_scale_f32_16x16x128_f8f6f4 v[186:189], v[16:23], v[56:63], v[186:189], v226, v227 op_sel_hi:[0,0,0]
	v_mfma_scale_f32_16x16x128_f8f6f4 v[182:185], v[24:31], v[48:55], v[182:185], v226, v227 op_sel_hi:[0,0,0]
	v_mfma_scale_f32_16x16x128_f8f6f4 v[174:177], v[16:23], v[48:55], v[174:177], v226, v227 op_sel_hi:[0,0,0]
	v_mfma_scale_f32_16x16x128_f8f6f4 v[166:169], v[24:31], v[40:47], v[166:169], v226, v227 op_sel_hi:[0,0,0]
	v_mfma_scale_f32_16x16x128_f8f6f4 v[158:161], v[16:23], v[40:47], v[158:161], v226, v227 op_sel_hi:[0,0,0]
	v_mfma_scale_f32_16x16x128_f8f6f4 v[150:153], v[24:31], v[32:39], v[150:153], v226, v227 op_sel_hi:[0,0,0]
	v_mfma_scale_f32_16x16x128_f8f6f4 v[142:145], v[16:23], v[32:39], v[142:145], v226, v227 op_sel_hi:[0,0,0]
	s_setprio 0
	s_setprio 1
	v_mfma_scale_f32_16x16x128_f8f6f4 v[178:181], v[8:15], v[56:63], v[178:181], v226, v227 op_sel_hi:[0,0,0]
	v_mfma_scale_f32_16x16x128_f8f6f4 v[170:173], v[0:7], v[56:63], v[170:173], v226, v227 op_sel_hi:[0,0,0]
	v_mfma_scale_f32_16x16x128_f8f6f4 v[162:165], v[8:15], v[48:55], v[162:165], v226, v227 op_sel_hi:[0,0,0]
	v_mfma_scale_f32_16x16x128_f8f6f4 v[154:157], v[0:7], v[48:55], v[154:157], v226, v227 op_sel_hi:[0,0,0]
	v_mfma_scale_f32_16x16x128_f8f6f4 v[146:149], v[8:15], v[40:47], v[146:149], v226, v227 op_sel_hi:[0,0,0]
	v_mfma_scale_f32_16x16x128_f8f6f4 v[138:141], v[0:7], v[40:47], v[138:141], v226, v227 op_sel_hi:[0,0,0]
	v_mfma_scale_f32_16x16x128_f8f6f4 v[134:137], v[8:15], v[32:39], v[134:137], v226, v227 op_sel_hi:[0,0,0]
	v_mfma_scale_f32_16x16x128_f8f6f4 v[130:133], v[0:7], v[32:39], v[130:133], v226, v227 op_sel_hi:[0,0,0]
	s_setprio 0
	s_barrier
	s_mov_b32 m0, s25
	v_lshl_add_u64 v[214:215], s[16:17], 0, v[194:195]
	s_add_u32 s2, s16, 0x2000
	ds_read_b128 v[56:59], v220 offset:16384
	ds_read_b128 v[60:63], v220 offset:17408
	ds_read_b128 v[48:51], v220 offset:18432
	ds_read_b128 v[52:55], v220 offset:19456
	ds_read_b128 v[40:43], v220 offset:20480
	ds_read_b128 v[44:47], v220 offset:21504
	ds_read_b128 v[32:35], v220 offset:22528
	ds_read_b128 v[36:39], v220 offset:23552
	global_load_lds_dwordx4 v[214:215], off
	v_lshl_add_u64 v[214:215], s[16:17], 0, v[200:201]
	s_mov_b32 m0, s26
	s_addc_u32 s3, s17, 0
	global_load_lds_dwordx4 v[214:215], off
	v_lshl_add_u64 v[232:233], s[2:3], 0, v[194:195]
	v_lshl_add_u64 v[216:217], s[18:19], 0, v[202:203]
	v_lshl_add_u64 v[234:235], s[2:3], 0, v[200:201]
	v_cndmask_b32_e64 v221, 0, 1, s[20:21]
	v_lshl_add_u64 v[214:215], s[18:19], 0, v[196:197]
	s_mov_b32 m0, s24
	v_cmp_ne_u32_e64 s[2:3], 1, v221
	global_load_lds_dwordx4 v[214:215], off
	s_mov_b32 m0, s29
	s_andn2_b64 vcc, exec, s[20:21]
	global_load_lds_dwordx4 v[216:217], off
	s_cbranch_vccnz .LBB0_804
	s_waitcnt vmcnt(22)
	s_cbranch_execnz .LBB0_801

; #define PG8_STAGE_A(bufoff, gbase, VO, h) do { _Pragma("unroll") for (int _i = 0; _i < 2; ++_i) \
;         __builtin_amdgcn_global_load_lds((const unsigned*)((const char*)(gbase) + (VO)[h][_i]), (LAS unsigned*)(lds + (bufoff) + ldsw + _i * 8192), 16, 0, 0); } while (0)
; #define PG8_WAIT_L(n) asm volatile("s_waitcnt lgkmcnt(" #n ")" ::: "memory")
; #define PG8_WAIT_VX(rx) do { if (rx) asm volatile("s_waitcnt vmcnt(%0)" :: "n"(8 + Epi::NVM) : "memory"); else asm volatile("s_waitcnt vmcnt(8)" ::: "memory"); } while (0)
; #define PG8_BAR __builtin_amdgcn_s_barrier()
; #define PG8_SCHED __builtin_amdgcn_sched_barrier(0)
;     ...
;             PG8_WAIT_VX(rx); PG8_WAIT_L(0); PG8_BAR; PG8_MMA(1, 0, At, B0); PG8_MMA(1, 1, At, B1); PG8_BAR; PG8_SCHED;
;             PG8_LDB(B0, 1, 0); PG8_LDB(B1, 1, 1); PG8_SCHED; PG8_LDA(At, 1, 0); PG8_STAGE_A(PG8_SA(0, 1), a2, vo2, 1);
.LBB0_801:
	s_waitcnt lgkmcnt(0)
	s_barrier
	s_setprio 1
	s_waitcnt lgkmcnt(0)
	v_mfma_scale_f32_16x16x128_f8f6f4 v[126:129], v[24:31], v[56:63], v[126:129], v226, v227 op_sel_hi:[0,0,0]
	v_mfma_scale_f32_16x16x128_f8f6f4 v[122:125], v[16:23], v[56:63], v[122:125], v226, v227 op_sel_hi:[0,0,0]
	v_mfma_scale_f32_16x16x128_f8f6f4 v[110:113], v[24:31], v[48:55], v[110:113], v226, v227 op_sel_hi:[0,0,0]
	v_mfma_scale_f32_16x16x128_f8f6f4 v[102:105], v[16:23], v[48:55], v[102:105], v226, v227 op_sel_hi:[0,0,0]
	v_mfma_scale_f32_16x16x128_f8f6f4 v[86:89], v[24:31], v[40:47], v[86:89], v226, v227 op_sel_hi:[0,0,0]
	v_mfma_scale_f32_16x16x128_f8f6f4 v[78:81], v[16:23], v[40:47], v[78:81], v226, v227 op_sel_hi:[0,0,0]
	v_mfma_scale_f32_16x16x128_f8f6f4 v[70:73], v[24:31], v[32:39], v[70:73], v226, v227 op_sel_hi:[0,0,0]
	v_mfma_scale_f32_16x16x128_f8f6f4 v[66:69], v[16:23], v[32:39], v[66:69], v226, v227 op_sel_hi:[0,0,0]
	s_setprio 0
	s_setprio 1
	v_mfma_scale_f32_16x16x128_f8f6f4 v[106:109], v[8:15], v[56:63], v[106:109], v226, v227 op_sel_hi:[0,0,0]
	v_mfma_scale_f32_16x16x128_f8f6f4 v[98:101], v[0:7], v[56:63], v[98:101], v226, v227 op_sel_hi:[0,0,0]
	v_mfma_scale_f32_16x16x128_f8f6f4 v[82:85], v[8:15], v[48:55], v[82:85], v226, v227 op_sel_hi:[0,0,0]
	v_mfma_scale_f32_16x16x128_f8f6f4 v[74:77], v[0:7], v[48:55], v[74:77], v226, v227 op_sel_hi:[0,0,0]
	v_mfma_scale_f32_16x16x128_f8f6f4 v[118:121], v[8:15], v[40:47], v[118:121], v226, v227 op_sel_hi:[0,0,0]
	v_mfma_scale_f32_16x16x128_f8f6f4 v[114:117], v[0:7], v[40:47], v[114:117], v226, v227 op_sel_hi:[0,0,0]
	v_mfma_scale_f32_16x16x128_f8f6f4 v[94:97], v[8:15], v[32:39], v[94:97], v226, v227 op_sel_hi:[0,0,0]
	v_mfma_scale_f32_16x16x128_f8f6f4 v[90:93], v[0:7], v[32:39], v[90:93], v226, v227 op_sel_hi:[0,0,0]
	s_setprio 0
	s_barrier
	v_add_u32_e32 v0, 0x18000, v219
	v_add_u32_e32 v4, 0x1c000, v219
	ds_read_b128 v[24:27], v0
	ds_read_b128 v[28:31], v0 offset:1024
	ds_read_b128 v[16:19], v0 offset:2048
	ds_read_b128 v[20:23], v0 offset:3072
	ds_read_b128 v[8:11], v4
	ds_read_b128 v[12:15], v4 offset:1024
	ds_read_b128 v[0:3], v4 offset:2048
	ds_read_b128 v[4:7], v4 offset:3072
	s_mov_b32 m0, s31
	v_lshl_add_u64 v[238:239], s[18:19], 0, v[198:199]
	ds_read_b128 v[56:59], v220 offset:32768
	ds_read_b128 v[60:63], v220 offset:33792
	ds_read_b128 v[48:51], v220 offset:34816
	ds_read_b128 v[52:55], v220 offset:35840
	ds_read_b128 v[40:43], v220 offset:36864
	ds_read_b128 v[44:47], v220 offset:37888
	ds_read_b128 v[32:35], v220 offset:38912
	ds_read_b128 v[36:39], v220 offset:39936
	s_mov_b32 m0, s27
	s_nop 0
	global_load_lds_dwordx4 v[232:233], off
	s_mov_b32 m0, s28
	s_nop 0
	global_load_lds_dwordx4 v[234:235], off
	s_mov_b32 m0, s31
	s_nop 0
	global_load_lds_dwordx4 v[238:239], off
	v_lshl_add_u64 v[238:239], s[18:19], 0, v[204:205]
	s_mov_b32 m0, s34
	s_and_b64 vcc, exec, s[2:3]
	global_load_lds_dwordx4 v[238:239], off
	s_cbranch_vccnz .LBB0_805
	s_waitcnt vmcnt(24)
	s_cbranch_execnz .LBB0_794
	s_branch .LBB0_806

; #define PG8_STAGE_A(bufoff, gbase, VO, h) do { _Pragma("unroll") for (int _i = 0; _i < 2; ++_i) \
;         __builtin_amdgcn_global_load_lds((const unsigned*)((const char*)(gbase) + (VO)[h][_i]), (LAS unsigned*)(lds + (bufoff) + ldsw + _i * 8192), 16, 0, 0); } while (0)
; #define PG8_BAR __builtin_amdgcn_s_barrier()
;     ...
;         if (ALIGN_EPI) { if (wr == 0) PG8_BAR; }
;         if (ALIGN_EPI && has_next) { if constexpr (GATHER) PG8_STAGE_A(PG8_SA(1, 1), nA + kstep, voffN, 1); else PG8_STAGE_A(PG8_SA(1, 1), nA + kstep, voffA, 1); }
.LBB0_809:
	v_cndmask_b32_e64 v0, 0, 1, s[12:13]
	v_cmp_ne_u32_e64 s[2:3], 1, v0
	s_andn2_b64 vcc, exec, s[12:13]
	s_cbranch_vccnz .LBB0_811
	v_lshl_add_u64 v[2:3], s[6:7], 0, v[198:199]
	v_lshl_add_u64 v[0:1], s[6:7], 0, v[204:205]
	v_lshl_add_u64 v[2:3], v[2:3], 0, s[94:95]
	s_mov_b32 m0, s41
	s_nop 0
	global_load_lds_dwordx4 v[232:233], off
	s_mov_b32 m0, s42
	s_nop 0
	global_load_lds_dwordx4 v[234:235], off
	s_add_i32 m0, s24, 0xc000
	v_lshl_add_u64 v[0:1], v[0:1], 0, s[94:95]
	global_load_lds_dwordx4 v[2:3], off
	s_add_i32 m0, s24, 0xe000
	s_nop 0
	global_load_lds_dwordx4 v[0:1], off
